# norm2 rows remapped to router block mapping; norm2-router grid barrier replaced by workgroup barrier
# speedup vs baseline: 1.0113x; 1.0113x over previous
; #define GAS __attribute__((address_space(1)))
; template <int MODE> DI void p_norm(Frame& F, const void* xin, const bool xbf, int comb_l, bf16* xout, const float* wn, const float* shift, const float* scale, bf16* hout, float* fout, const int blk = -1) {
;     const int gw0 = F.vcu * NWAVES + F.wave; const int gw = blk < 0 ? gw0 : blk * 128 + F.wave * 16, NGW = blk < 0 ? F.G * NWAVES : 1, TE = blk < 0 ? T : blk * 128 + F.wave * 16 + 16;
;     const float* mod = (const float*)(F.ws + WS_MOD);
;     const int* tokd = (const int*)(F.ws + WS_TOK + 768 * 1024); const float* tokw = (const float*)(F.ws + WS_TOK + 512 * 1024);
;     ...
;     const bf16* yb = (const bf16*)(F.ws + WS_XB);
;     ...
;     const bf16* yb = (const bf16*)(F.ws + WS_YB);
;     ...
;     const bool comb = comb_l >= 0;
;     f32x4 wv[4];
; #pragma unroll
;     for (int j = 0; j < 4; ++j) wv[j] = *((const f32x4*)wn + F.lane + 64 * j);
;     struct Tok { v2u d, w; };
;     struct Row { v2u xb[4]; f32x4 xf[4]; v2u ya[4], yc[4]; };
;     auto ld_tok = [&](const int m, Tok& t) { t.d = *(const v2u*)(tokd + 2 * m); t.w = *(const v2u*)((const unsigned*)tokw + 2 * m); };
;     auto ld_row = [&](const int m, const Tok& t, Row& R) {
;         if (xbf) { const GAS v2u* xr = (const GAS v2u*)((const bf16*)xin + (size_t)m * D) + F.lane;
; #pragma unroll
;             for (int j = 0; j < 4; ++j) R.xb[j] = __builtin_nontemporal_load(xr + 64 * j);
;         } else { const GAS f32x4* xr = (const GAS f32x4*)((const float*)xin + (size_t)m * D) + F.lane;
; #pragma unroll
;             for (int j = 0; j < 4; ++j) R.xf[j] = __builtin_nontemporal_load(xr + 64 * j); }
;         if (comb) {
; #pragma unroll
;             for (int j = 0; j < 4; ++j) { R.ya[j] = __builtin_nontemporal_load((const v2u*)(yb + (size_t)t.d[0] * 1024) + F.lane + 64 * j); R.yc[j] = __builtin_nontemporal_load((const v2u*)(yb + (size_t)t.d[1] * 1024) + F.lane + 64 * j); } } };
;     Tok tA, tB; Row RA;
;     tA.d = (v2u){0u, 0u}; tA.w = tA.d; tB = tA;
;     if (gw < TE) { if (comb) { ld_tok(gw, tA); if (gw + NGW < TE) ld_tok(gw + NGW, tB); } ld_row(gw, tA, RA); }
;     for (int m = gw; m < TE; m += NGW) {
;         Row RN; Tok tN; tN.d = (v2u){0u, 0u}; tN.w = tN.d;
;         if (m + NGW < TE) { ld_row(m + NGW, tB, RN); if (comb && m + 2 * NGW < TE) ld_tok(m + 2 * NGW, tN); }
;         const int b = m >> 13;
.LBB0_3232:
	s_add_i32 s8, s8, 0
	s_add_i32 s8, s8, 0x20890
	v_mov_b32_e32 v0, s8
	s_waitcnt lgkmcnt(0)
	ds_read2_b32 v[4:5], v0 offset1:1
	s_ashr_i32 s8, s3, 6
	s_lshl_b32 s8, s8, 4
	s_lshl_b32 s9, s57, 7
	s_add_i32 s12, s9, s8
	s_add_i32 s34, s12, 15
	s_cmpk_gt_i32 s12, 0x7fff
	s_waitcnt lgkmcnt(0)
	v_readfirstlane_b32 s7, v4
	v_readfirstlane_b32 s10, v5
	s_cbranch_scc1 .LBB0_3237
	v_readlane_b32 s16, v255, 3
	v_readlane_b32 s18, v255, 5
	v_readlane_b32 s19, v255, 6
	s_add_u32 s14, s18, s0
	s_addc_u32 s15, s19, s1
	s_ashr_i32 s3, s2, 31
	s_lshl_b64 s[0:1], s[2:3], 12
	s_waitcnt vmcnt(0)
	v_and_b32_e32 v22, 63, v1
	s_add_u32 s0, s7, s0
	s_addc_u32 s1, s10, s1
	v_lshlrev_b32_e32 v2, 4, v22
	global_load_dwordx4 v[4:7], v2, s[0:1]
	global_load_dwordx4 v[8:11], v2, s[0:1] offset:1024
	global_load_dwordx4 v[12:15], v2, s[0:1] offset:2048
	global_load_dwordx4 v[16:19], v2, s[0:1] offset:3072
	s_mov_b32 s0, 1
	s_mul_hi_i32 s1, s2, 0x18000
	s_mul_i32 s2, s2, 0x18000
	s_add_u32 s2, s14, s2
	s_addc_u32 s3, s15, s1
	s_ashr_i32 s13, s12, 31
	s_lshl_b64 s[6:7], s[12:13], 11
	s_add_u32 s6, s14, s6
	s_addc_u32 s7, s15, s7
	v_lshlrev_b32_e32 v24, 3, v22
	v_mov_b32_e32 v25, v3
	v_lshl_add_u64 v[0:1], s[6:7], 0, v[24:25]
	s_mov_b64 s[6:7], 0x3d900000
	s_mov_b32 s1, 0x3d900000
	v_lshl_add_u64 v[20:21], v[0:1], 0, s[6:7]
	v_add_co_u32_e32 v0, vcc, s1, v0
	s_add_i32 s1, s8, s0
	s_nop 0
	v_addc_co_u32_e32 v1, vcc, 0, v1, vcc
	global_load_dwordx2 v[42:43], v[0:1], off nt
	global_load_dwordx2 v[44:45], v[20:21], off offset:512 nt
	global_load_dwordx2 v[40:41], v[20:21], off offset:1024 nt
	global_load_dwordx2 v[36:37], v[20:21], off offset:1536 nt
	v_lshlrev_b32_e32 v0, 2, v22
	v_lshl_add_u64 v[22:23], s[2:3], 0, v[2:3]
	s_mov_b64 s[2:3], 0x104000
	v_lshl_add_u64 v[20:21], v[22:23], 0, s[2:3]
	s_mov_b64 s[2:3], 0x103000
	v_lshl_add_u64 v[22:23], v[22:23], 0, s[2:3]
	s_add_i32 s2, s1, s9
	s_ashr_i32 s3, s2, 31
	s_lshl_b64 s[2:3], s[2:3], 11
	s_add_u32 s2, s2, 0x3d900400
	s_addc_u32 s3, s3, 0
	s_ashr_i32 s1, s0, 31
	s_lshl_b64 s[6:7], s[0:1], 11
	s_ashr_i32 s1, s8, 31
	s_ashr_i32 s10, s9, 31
	s_add_u32 s8, s8, s9
	s_addc_u32 s9, s1, s10
	s_lshl_b64 s[8:9], s[8:9], 11
	s_add_u32 s8, s8, 0x7100400
	v_xor_b32_e32 v1, 4, v0
	v_xor_b32_e32 v56, 8, v0
	v_xor_b32_e32 v57, 16, v0
	v_xor_b32_e32 v58, 32, v0
	v_xor_b32_e32 v59, 64, v0
	v_xor_b32_e32 v60, 0x80, v0
	v_lshl_add_u64 v[24:25], s[14:15], 0, v[24:25]
	s_addc_u32 s9, s9, 0
	v_readlane_b32 s17, v255, 4
	s_branch .LBB0_3235

; __device__ __forceinline__ unsigned xb_ld(unsigned* p)              { return __hip_atomic_load(p, __ATOMIC_RELAXED, __HIP_MEMORY_SCOPE_AGENT); }
; __device__ __forceinline__ unsigned xb_add(unsigned* p, unsigned v) { return __hip_atomic_fetch_add(p, v, __ATOMIC_RELAXED, __HIP_MEMORY_SCOPE_AGENT); }
; #define XB_SPIN(cond, bar) do { unsigned _sp = 0; while (cond) { __builtin_amdgcn_s_sleep(1); \
;     if ((++_sp & 255u) == 0u) { if (xb_ld(&(bar)[XB_TMO])) break; if (_sp > XB_SPIN_CAP) { atomicAdd(&(bar)[XB_TMO], 1u); break; } } } } while (0)
; __device__ __forceinline__ void xcd_barrier(const XcdBarrier& b) {
;     asm volatile("s_waitcnt vmcnt(0)" ::: "memory");
;     __syncthreads();
;     if (threadIdx.x == 0) {
;         unsigned* bar = b.bar;
;         __builtin_amdgcn_s_waitcnt(0);
;         unsigned nloc = b.st[0], nx = b.st[1];
;         if (nloc == 0u) { xcd_barrier_complete(bar, b.x, nloc, nx); b.st[0] = nloc; b.st[1] = nx; }
;         const unsigned old = xb_add(&bar[XB_XSUB(b.x)], 1u);
;         const unsigned gen = old / nloc;
;         if (old + 1u == (gen + 1u) * nloc) {
;             __builtin_amdgcn_fence(__ATOMIC_RELEASE, XB_SCOPE);
;             asm volatile("s_waitcnt vmcnt(0)" ::: "memory");
;             const unsigned og = xb_add(&bar[XB_TOP], 1u);
;             const unsigned tg = og / nx;
;             if (og + 1u == (tg + 1u) * nx) xb_add(&bar[XB_TOPGEN], 1u);
;             else XB_SPIN(xb_ld(&bar[XB_TOPGEN]) == tg, bar);
;             __builtin_amdgcn_fence(__ATOMIC_ACQUIRE, XB_SCOPE);
;             xb_add(&bar[XB_XGEN(b.x)], 1u);
;             asm volatile("s_waitcnt vmcnt(0)" ::: "memory");
;         } else {
;             XB_SPIN(xb_ld(&bar[XB_XGEN(b.x)]) == gen, bar);
;             __builtin_amdgcn_fence(__ATOMIC_ACQUIRE, XB_SCOPE);
;             asm volatile("s_waitcnt vmcnt(0)" ::: "memory");
;         }
;     }
;     __syncthreads();
; }
; template <int MODE> DI void p_norm(Frame& F, const void* xin, const bool xbf, int comb_l, bf16* xout, const float* wn, const float* shift, const float* scale, bf16* hout, float* fout, const int blk = -1) {
;     ...
;     for (int m = gw; m < TE; m += NGW) {
;         Row RN; Tok tN; tN.d = (v2u){0u, 0u}; tN.w = tN.d;
;         if (m + NGW < TE) { ld_row(m + NGW, tB, RN); if (comb && m + 2 * NGW < TE) ld_tok(m + 2 * NGW, tN); }
.LBB0_3235:
	s_add_i32 s1, s12, s0
	s_cmp_gt_i32 s1, s34
	s_cselect_b64 s[10:11], -1, 0
	s_and_b64 vcc, exec, s[10:11]
	s_cbranch_vccnz .LBB0_3234
	v_lshl_add_u64 v[32:33], v[24:25], 0, s[2:3]
	global_load_dwordx2 v[26:27], v[32:33], off offset:-1024 nt
	global_load_dwordx2 v[28:29], v[32:33], off offset:-512 nt
	global_load_dwordx2 v[30:31], v[32:33], off nt
	s_nop 0
	global_load_dwordx2 v[32:33], v[32:33], off offset:512 nt
	s_branch .LBB0_3234
.LBB0_3237:
	v_readlane_b32 s0, v255, 14
	s_add_i32 s50, s0, 7
	v_readlane_b32 s0, v255, 10
	v_readlane_b32 s1, v255, 11
	s_cmp_lt_i32 s50, s1
	s_cselect_b64 s[0:1], -1, 0
	s_and_b64 s[2:3], s[4:5], s[0:1]
	s_andn2_b64 vcc, exec, s[2:3]
	s_waitcnt vmcnt(0) lgkmcnt(0)
	s_barrier
	s_branch .LBB0_3291
